# code self-prefetch range of the last kernel trimmed to stay inside .text
# baseline (speedup 1.0000x reference)
.Lw3b0:
	s_and_b32 s58, s58, 0xffffff00
	v_lshlrev_b32_e32 v48, 7, v0
	v_cmp_gt_u32_e32 vcc, 0x3000, v48
	s_and_saveexec_b64 s[60:61], vcc
	global_load_dword v127, v48, s[58:59]
	s_or_b64 exec, exec, s[60:61]
	s_load_dwordx4 s[12:15], s[0:1], 0x38
	s_load_dwordx8 s[4:11], s[0:1], 0x18
	v_lshlrev_b32_e32 v2, 4, v0
	v_min_u32_e32 v1, 0x7f, v0
	v_lshlrev_b32_e32 v26, 2, v1
	v_readfirstlane_b32 s3, v0
	v_add_u32_e32 v28, 0x3400, v2
	v_add_u32_e32 v29, 0x6800, v2
	v_add_u32_e32 v30, 0x9c00, v2
	v_add_u32_e32 v31, 0xd00, v0
	v_min_u32_e32 v31, 0xfff, v31
	v_lshlrev_b32_e32 v31, 4, v31
	v_add_u32_e32 v27, 0x680, v0
